# fixup kernel arguments and work-list entry fetched in two scalar round trips instead of three, on top of the hand-written spatial kernel
# baseline (speedup 1.0000x reference)
_Z7k_fixupPKfS0_S0_PDF16_S1_S1_PfPKi:
	s_load_dwordx2 s[34:35], s[0:1], 0x38
	s_load_dwordx8 s[20:27], s[0:1], 0x0
	s_load_dwordx4 s[28:31], s[0:1], 0x20
	s_load_dwordx2 s[36:37], s[0:1], 0x30
	s_lshl_b32 s38, s2, 2
	s_waitcnt lgkmcnt(0)
	s_load_dword s33, s[34:35], 0x0
	s_add_u32 s38, s34, s38
	s_addc_u32 s39, s35, 0
	s_load_dword s59, s[38:39], 0x10
	s_waitcnt lgkmcnt(0)
	s_cmp_ge_i32 s2, s33
	s_cbranch_scc1 .LBB2_52
	v_and_b32_e32 v1, 15, v0
	v_mul_u32_u24_e32 v7, 0xe38f, v0
	v_lshlrev_b32_e32 v2, 2, v1
	s_movk_i32 s3, 0xc0
	v_min_u32_e32 v4, 8, v1
	v_lshrrev_b32_e32 v118, 19, v7
	v_and_or_b32 v3, v0, s3, v2
	v_mul_u32_u24_e32 v116, 0x628, v4
	v_lshrrev_b32_e32 v4, 2, v0
	v_lshlrev_b32_e32 v5, 2, v0
	s_movk_i32 s3, 0xe00
	v_mul_u32_u24_e32 v7, 9, v118
	v_lshrrev_b32_e32 v89, 6, v0
	v_and_b32_e32 v4, 12, v4
	v_and_or_b32 v117, v5, s3, v1
	s_movk_i32 s3, 0x51
	v_lshlrev_b32_e32 v8, 3, v0
	v_lshlrev_b32_e32 v9, 3, v7
	v_lshlrev_b32_e32 v82, 2, v4
	v_mov_b32_e32 v83, 0
	v_lshlrev_b32_e32 v6, 5, v89
	v_cmp_gt_u32_e64 s[18:19], s3, v0
	v_add_u32_e32 v119, 0x2140, v8
	v_add_u32_e32 v120, 0x2140, v9
	v_add_u32_e32 v121, 0x1c20, v8
	v_add_u32_e32 v122, 0x1c20, v9
	v_add_u32_e32 v123, 0x1eb0, v8
	v_add_u32_e32 v124, 0x1eb0, v9
	v_cmp_eq_u32_e32 vcc, v0, v7
	v_cmp_lt_u32_e64 s[4:5], 8, v0
	v_mov_b32_e32 v8, 0x2518
	v_add_u32_e32 v126, 0x23d0, v5
	v_lshlrev_b32_e32 v5, 4, v89
	s_movk_i32 s3, 0x400
	v_or_b32_e32 v9, 1, v4
	s_waitcnt lgkmcnt(0)
	v_lshl_add_u64 v[84:85], s[20:21], 0, v[82:83]
	s_and_b64 s[20:21], vcc, s[4:5]
	v_lshl_add_u32 v125, v118, 3, v8
	v_or3_b32 v127, v1, v5, s3
	v_and_b32_e32 v5, 63, v0
	v_lshrrev_b32_e32 v8, 1, v0
	v_and_b32_e32 v129, 32, v6
	v_cmp_gt_u32_e64 s[12:13], 9, v9
	v_or_b32_e32 v9, 2, v4
	v_bitop3_b32 v130, v6, 48, 16 bitop3:0xc8
	v_mul_u32_u24_e32 v6, 0x210, v0
	v_mul_u32_u24_e32 v7, 0x210, v7
	v_lshl_add_u64 v[86:87], s[22:23], 0, v[82:83]
	v_add_u32_e32 v3, 0x1290, v3
	s_movk_i32 s3, 0x1c0
	s_add_u32 s22, s0, 64
	v_and_b32_e32 v128, 32, v8
	v_lshl_or_b32 v2, v89, 7, v2
	v_cmp_gt_u32_e64 s[10:11], 9, v4
	v_mul_u32_u24_e32 v8, 0x210, v4
	v_cmp_gt_u32_e64 s[14:15], 9, v9
	v_or_b32_e32 v9, 3, v4
	v_mul_u32_u24_e32 v4, 0x110, v4
	v_lshlrev_b32_e32 v88, 2, v5
	v_sub_u32_e32 v6, v6, v7
	s_mov_b32 s40, 0x652b82fe
	s_mov_b32 s42, 0xfefa39ef
	s_mov_b32 s44, 0x3b39803f
	s_mov_b32 s46, 0x6a5dcb37
	s_mov_b32 s48, 0
	s_mov_b32 s50, 0
	s_mov_b32 s52, 0x1c71c71c
	s_movk_i32 s78, 0x210
	s_mov_b32 s39, 0
	v_cmp_eq_u32_e64 s[4:5], 0, v0
	v_cmp_gt_u32_e64 s[6:7], s3, v0
	v_cmp_gt_u32_e64 s[8:9], 54, v0
	v_mov_b32_e32 v1, v83
	s_addc_u32 s23, s1, 0
	v_cmp_gt_u32_e64 s[16:17], 9, v9
	v_add_u32_e32 v131, 0x1290, v88
	v_add_u32_e32 v132, 0x100, v6
	v_sub_u32_e32 v133, 0, v89
	v_lshlrev_b32_e32 v90, 1, v5
	v_mov_b32_e32 v91, v83
	s_mov_b32 s41, 0x3ff71547
	s_mov_b32 s43, 0xbfe62e42
	s_mov_b32 s45, 0xbc7abc9e
	s_mov_b32 s47, 0x3e5ade15
	s_mov_b32 s49, 0x40900000
	s_mov_b32 s51, 0xc090cc00
	s_mov_b32 s53, 0xbfbc71c7
	s_movk_i32 s79, 0xc5
	s_mov_b64 s[54:55], 0x18a00
	s_movk_i32 s80, 0xbf
	v_add_u32_e32 v134, v2, v8
	v_mov_b32_e32 v92, 0xfca7ab0c
	v_mov_b32_e32 v93, 0x3e928af3
	v_mov_b32_e32 v94, 0x623fde64
	v_mov_b32_e32 v95, 0x3ec71dee
	v_mov_b32_e32 v96, 0x7c89e6b0
	v_mov_b32_e32 v97, 0x3efa0199
	v_mov_b32_e32 v98, 0x14761f6e
	v_mov_b32_e32 v99, 0x3f2a01a0
	v_mov_b32_e32 v100, 0x1852b7b0
	v_mov_b32_e32 v101, 0x3f56c16c
	v_mov_b32_e32 v102, 0x11122322
	v_mov_b32_e32 v103, 0x3f811111
	v_mov_b32_e32 v104, 0x555502a1
	v_mov_b32_e32 v105, 0x3fa55555
	v_mov_b32_e32 v106, 0x55555511
	v_mov_b32_e32 v107, 0x3fc55555
	v_mov_b32_e32 v108, 11
	v_mov_b32_e32 v109, 0x3fe00000
	v_add_u32_e32 v135, v3, v4
	v_mov_b32_e32 v136, 0x40a00000
	v_mov_b32_e32 v137, 0x40c00000
	v_mov_b32_e32 v138, 0x40e00000
	s_branch .Lfix_first

.Lfix_first:
	v_or_b32_e32 v3, 16, v128
	s_waitcnt lgkmcnt(0)
	s_ashr_i32 s3, s59, 16
	s_lshl_b32 s58, s3, 6
	v_add_u32_e32 v139, s58, v117
	s_and_b32 s38, s59, 0xffff
	v_or_b32_e32 v2, v128, v139
	v_or_b32_e32 v4, v139, v3
	v_ashrrev_i32_e32 v3, 31, v2
	v_ashrrev_i32_e32 v5, 31, v4
	v_add_lshl_u32 v82, s38, v116, 11
	v_lshlrev_b64 v[2:3], 11, v[2:3]
	v_lshlrev_b64 v[4:5], 11, v[4:5]
	v_lshl_add_u64 v[110:111], v[84:85], 0, v[82:83]
	v_lshl_add_u64 v[114:115], v[86:87], 0, v[2:3]
	v_lshl_add_u64 v[112:113], v[86:87], 0, v[4:5]
	global_load_dwordx4 v[2:5], v[110:111], off nt
	global_load_dwordx4 v[10:13], v[110:111], off offset:64 nt
	global_load_dwordx4 v[22:25], v[114:115], off
	global_load_dwordx4 v[26:29], v[114:115], off offset:64
	global_load_dwordx4 v[34:37], v[112:113], off
	global_load_dwordx4 v[46:49], v[112:113], off offset:64
	global_load_dwordx4 v[50:53], v[110:111], off offset:128 nt
	global_load_dwordx4 v[70:73], v[110:111], off offset:192 nt
	global_load_dwordx4 v[74:77], v[114:115], off offset:128
	global_load_dwordx4 v[78:81], v[114:115], off offset:192
	global_load_dwordx4 v[140:143], v[112:113], off offset:128
	global_load_dwordx4 v[144:147], v[112:113], off offset:192
	global_load_dwordx4 v[54:57], v[110:111], off offset:256 nt
	global_load_dwordx4 v[38:41], v[110:111], off offset:320 nt
	global_load_dwordx4 v[148:151], v[114:115], off offset:256
	global_load_dwordx4 v[66:69], v[114:115], off offset:320
	global_load_dwordx4 v[152:155], v[112:113], off offset:256
	global_load_dwordx4 v[58:61], v[112:113], off offset:320
	global_load_dwordx4 v[18:21], v[110:111], off offset:384 nt
	global_load_dwordx4 v[6:9], v[110:111], off offset:448 nt
	global_load_dwordx4 v[42:45], v[114:115], off offset:384
	global_load_dwordx4 v[14:17], v[114:115], off offset:448
	global_load_dwordx4 v[62:65], v[112:113], off offset:384
	global_load_dwordx4 v[30:33], v[112:113], off offset:448
	s_waitcnt vmcnt(23)
	s_waitcnt vmcnt(21)
	s_nop 0
	v_mfma_f32_16x16x4_f32 a[0:3], v2, v22, 0
	s_waitcnt vmcnt(19)
	v_mov_b32_e32 v22, v34
	v_mov_b32_e32 v34, v36
	s_nop 0
	v_mfma_f32_16x16x4_f32 a[4:7], v2, v22, 0
	v_mov_b32_e32 v2, v11
	v_mov_b32_e32 v11, v28
	s_waitcnt vmcnt(18)
	v_mov_b32_e32 v22, v49
	v_mfma_f32_16x16x4_f32 a[0:3], v3, v23, a[0:3]
	v_mfma_f32_16x16x4_f32 a[4:7], v3, v35, a[4:7]
	v_mov_b32_e32 v3, v13
	v_mov_b32_e32 v13, v47
	v_mfma_f32_16x16x4_f32 a[0:3], v4, v24, a[0:3]
	v_mfma_f32_16x16x4_f32 a[4:7], v4, v34, a[4:7]
	v_mov_b32_e32 v4, v10
	v_mov_b32_e32 v10, v26
	v_mfma_f32_16x16x4_f32 a[0:3], v5, v25, a[0:3]
	v_mfma_f32_16x16x4_f32 a[4:7], v5, v37, a[4:7]
	v_mov_b32_e32 v5, v29
	s_nop 0
	v_mfma_f32_16x16x4_f32 a[0:3], v4, v10, a[0:3]
	v_mov_b32_e32 v10, v48
	s_nop 0
	v_mfma_f32_16x16x4_f32 a[4:7], v4, v46, a[4:7]
	s_waitcnt vmcnt(17)
	v_mov_b32_e32 v4, v50
	v_mfma_f32_16x16x4_f32 a[0:3], v2, v27, a[0:3]
	v_mfma_f32_16x16x4_f32 a[4:7], v2, v13, a[4:7]
	v_mov_b32_e32 v2, v51
	s_waitcnt vmcnt(13)
	v_mov_b32_e32 v13, v143
	v_mfma_f32_16x16x4_f32 a[0:3], v12, v11, a[0:3]
	v_mov_b32_e32 v11, v76
	v_mfma_f32_16x16x4_f32 a[4:7], v12, v10, a[4:7]
	v_mov_b32_e32 v10, v74
	v_mov_b32_e32 v12, v141
	v_mfma_f32_16x16x4_f32 a[0:3], v3, v5, a[0:3]
	v_mov_b32_e32 v5, v77
	v_mfma_f32_16x16x4_f32 a[4:7], v3, v22, a[4:7]
	v_mov_b32_e32 v3, v53
	s_nop 0
	v_mfma_f32_16x16x4_f32 a[0:3], v4, v10, a[0:3]
	v_mov_b32_e32 v10, v142
	s_nop 0
	v_mfma_f32_16x16x4_f32 a[4:7], v4, v140, a[4:7]
	v_mov_b32_e32 v4, v72
	v_mfma_f32_16x16x4_f32 a[0:3], v2, v75, a[0:3]
	v_mfma_f32_16x16x4_f32 a[4:7], v2, v12, a[4:7]
	v_mov_b32_e32 v2, v73
	s_waitcnt vmcnt(12)
	v_mov_b32_e32 v12, v147
	v_mfma_f32_16x16x4_f32 a[0:3], v52, v11, a[0:3]
	v_mov_b32_e32 v11, v79
	v_mfma_f32_16x16x4_f32 a[4:7], v52, v10, a[4:7]
	v_mov_b32_e32 v10, v80
	v_mfma_f32_16x16x4_f32 a[0:3], v3, v5, a[0:3]
	v_mov_b32_e32 v5, v78
	v_mfma_f32_16x16x4_f32 a[4:7], v3, v13, a[4:7]
	v_mov_b32_e32 v3, v70
	v_mov_b32_e32 v13, v144
	s_nop 0
	v_mfma_f32_16x16x4_f32 a[0:3], v3, v5, a[0:3]
	v_mov_b32_e32 v5, v145
	s_nop 0
	v_mfma_f32_16x16x4_f32 a[4:7], v3, v13, a[4:7]
	v_mfma_f32_16x16x4_f32 a[0:3], v71, v11, a[0:3]
	v_mfma_f32_16x16x4_f32 a[4:7], v71, v5, a[4:7]
	v_mfma_f32_16x16x4_f32 a[0:3], v4, v10, a[0:3]
	v_mfma_f32_16x16x4_f32 a[4:7], v4, v146, a[4:7]
	v_mfma_f32_16x16x4_f32 a[0:3], v2, v81, a[0:3]
	v_mfma_f32_16x16x4_f32 a[4:7], v2, v12, a[4:7]
	global_load_dwordx4 v[70:73], v[110:111], off offset:512 nt
	global_load_dwordx4 v[34:37], v[110:111], off offset:576 nt
	global_load_dwordx4 v[140:143], v[114:115], off offset:512
	global_load_dwordx4 v[46:49], v[114:115], off offset:576
	global_load_dwordx4 v[144:147], v[112:113], off offset:512
	global_load_dwordx4 v[74:77], v[112:113], off offset:576
	global_load_dwordx4 v[22:25], v[110:111], off offset:640 nt
	global_load_dwordx4 v[2:5], v[110:111], off offset:704 nt
	global_load_dwordx4 v[50:53], v[114:115], off offset:640
	global_load_dwordx4 v[10:13], v[114:115], off offset:704
	global_load_dwordx4 v[78:81], v[112:113], off offset:640
	global_load_dwordx4 v[26:29], v[112:113], off offset:704
	s_waitcnt vmcnt(21)
	v_mov_b32_e32 v82, v150
	v_mov_b32_e32 v150, v151
	s_waitcnt vmcnt(19)
	v_mov_b32_e32 v151, v155
	v_mfma_f32_16x16x4_f32 a[0:3], v54, v148, a[0:3]
	v_mov_b32_e32 v148, v153
	s_nop 0
	v_mfma_f32_16x16x4_f32 a[4:7], v54, v152, a[4:7]
	v_mov_b32_e32 v54, v68
	v_mfma_f32_16x16x4_f32 a[0:3], v55, v149, a[0:3]
	v_mfma_f32_16x16x4_f32 a[4:7], v55, v148, a[4:7]
	v_mov_b32_e32 v55, v67
	v_mfma_f32_16x16x4_f32 a[0:3], v56, v82, a[0:3]
	v_mfma_f32_16x16x4_f32 a[4:7], v56, v154, a[4:7]
	v_mov_b32_e32 v56, v69
	v_mfma_f32_16x16x4_f32 a[0:3], v57, v150, a[0:3]
	v_mfma_f32_16x16x4_f32 a[4:7], v57, v151, a[4:7]
	s_waitcnt vmcnt(18)
	v_mov_b32_e32 v57, v61
	s_waitcnt vmcnt(17)
	v_mfma_f32_16x16x4_f32 a[0:3], v38, v66, a[0:3]
	v_mfma_f32_16x16x4_f32 a[4:7], v38, v58, a[4:7]
	s_waitcnt vmcnt(15)
	v_mov_b32_e32 v38, v43
	v_mfma_f32_16x16x4_f32 a[0:3], v39, v55, a[0:3]
	v_mfma_f32_16x16x4_f32 a[4:7], v39, v59, a[4:7]
	v_mov_b32_e32 v39, v45
	v_mfma_f32_16x16x4_f32 a[0:3], v40, v54, a[0:3]
	v_mfma_f32_16x16x4_f32 a[4:7], v40, v60, a[4:7]
	v_mov_b32_e32 v40, v42
	s_waitcnt vmcnt(13)
	v_mov_b32_e32 v42, v64
	v_mfma_f32_16x16x4_f32 a[0:3], v41, v56, a[0:3]
	v_mfma_f32_16x16x4_f32 a[4:7], v41, v57, a[4:7]
	v_mov_b32_e32 v41, v62
	v_mfma_f32_16x16x4_f32 a[0:3], v18, v40, a[0:3]
	v_mov_b32_e32 v40, v65
	s_nop 0
	v_mfma_f32_16x16x4_f32 a[4:7], v18, v41, a[4:7]
	s_waitcnt vmcnt(12)
	v_mov_b32_e32 v18, v30
	v_mfma_f32_16x16x4_f32 a[0:3], v19, v38, a[0:3]
	v_mfma_f32_16x16x4_f32 a[4:7], v19, v63, a[4:7]
	v_mov_b32_e32 v19, v32
	v_mfma_f32_16x16x4_f32 a[0:3], v20, v44, a[0:3]
	v_mfma_f32_16x16x4_f32 a[4:7], v20, v42, a[4:7]
	v_mfma_f32_16x16x4_f32 a[0:3], v21, v39, a[0:3]
	v_mfma_f32_16x16x4_f32 a[4:7], v21, v40, a[4:7]
	v_mfma_f32_16x16x4_f32 a[0:3], v6, v14, a[0:3]
	v_mov_b32_e32 v14, v33
	s_nop 0
	v_mfma_f32_16x16x4_f32 a[4:7], v6, v18, a[4:7]
	v_mfma_f32_16x16x4_f32 a[0:3], v7, v15, a[0:3]
	v_mfma_f32_16x16x4_f32 a[4:7], v7, v31, a[4:7]
	v_mfma_f32_16x16x4_f32 a[0:3], v8, v16, a[0:3]
	v_mfma_f32_16x16x4_f32 a[4:7], v8, v19, a[4:7]
	v_mfma_f32_16x16x4_f32 a[0:3], v9, v17, a[0:3]
	v_mfma_f32_16x16x4_f32 a[4:7], v9, v14, a[4:7]
	global_load_dwordx4 v[54:57], v[110:111], off offset:768 nt
	global_load_dwordx4 v[38:41], v[110:111], off offset:832 nt
	global_load_dwordx4 v[148:151], v[114:115], off offset:768
	global_load_dwordx4 v[66:69], v[114:115], off offset:832
	global_load_dwordx4 v[152:155], v[112:113], off offset:768
	global_load_dwordx4 v[58:61], v[112:113], off offset:832
	global_load_dwordx4 v[18:21], v[110:111], off offset:896 nt
	global_load_dwordx4 v[6:9], v[110:111], off offset:960 nt
	global_load_dwordx4 v[42:45], v[114:115], off offset:896
	global_load_dwordx4 v[14:17], v[114:115], off offset:960
	global_load_dwordx4 v[62:65], v[112:113], off offset:896
	global_load_dwordx4 v[30:33], v[112:113], off offset:960
	s_waitcnt vmcnt(21)
	v_mov_b32_e32 v82, v143
	s_waitcnt vmcnt(19)
	v_mov_b32_e32 v143, v146
	v_mfma_f32_16x16x4_f32 a[0:3], v70, v140, a[0:3]
	v_mov_b32_e32 v140, v144
	v_mov_b32_e32 v144, v145
	s_nop 0
	v_mfma_f32_16x16x4_f32 a[4:7], v70, v140, a[4:7]
	s_waitcnt vmcnt(18)
	v_mov_b32_e32 v70, v75
	v_mfma_f32_16x16x4_f32 a[0:3], v71, v141, a[0:3]
	v_mfma_f32_16x16x4_f32 a[4:7], v71, v144, a[4:7]
	v_mov_b32_e32 v71, v77
	v_mfma_f32_16x16x4_f32 a[0:3], v72, v142, a[0:3]
	v_mfma_f32_16x16x4_f32 a[4:7], v72, v143, a[4:7]
	v_mfma_f32_16x16x4_f32 a[0:3], v73, v82, a[0:3]
	v_mfma_f32_16x16x4_f32 a[4:7], v73, v147, a[4:7]
	v_mfma_f32_16x16x4_f32 a[0:3], v34, v46, a[0:3]
	v_mov_b32_e32 v46, v76
	s_waitcnt vmcnt(17)
	v_mfma_f32_16x16x4_f32 a[4:7], v34, v74, a[4:7]
	s_waitcnt vmcnt(15)
	v_mov_b32_e32 v34, v53
	v_mfma_f32_16x16x4_f32 a[0:3], v35, v47, a[0:3]
	v_mfma_f32_16x16x4_f32 a[4:7], v35, v70, a[4:7]
	v_mov_b32_e32 v35, v50
	v_mfma_f32_16x16x4_f32 a[0:3], v36, v48, a[0:3]
	v_mfma_f32_16x16x4_f32 a[4:7], v36, v46, a[4:7]
	v_mov_b32_e32 v36, v52
	s_waitcnt vmcnt(13)
	v_mov_b32_e32 v46, v81
	v_mfma_f32_16x16x4_f32 a[0:3], v37, v49, a[0:3]
	v_mfma_f32_16x16x4_f32 a[4:7], v37, v71, a[4:7]
	v_mov_b32_e32 v37, v79
	v_mfma_f32_16x16x4_f32 a[0:3], v22, v35, a[0:3]
	v_mov_b32_e32 v35, v80
	s_nop 0
	v_mfma_f32_16x16x4_f32 a[4:7], v22, v78, a[4:7]
	s_waitcnt vmcnt(12)
	v_mov_b32_e32 v22, v29
	v_mfma_f32_16x16x4_f32 a[0:3], v23, v51, a[0:3]
	v_mfma_f32_16x16x4_f32 a[4:7], v23, v37, a[4:7]
	v_mov_b32_e32 v23, v26
	v_mfma_f32_16x16x4_f32 a[0:3], v24, v36, a[0:3]
	v_mfma_f32_16x16x4_f32 a[4:7], v24, v35, a[4:7]
	v_mfma_f32_16x16x4_f32 a[0:3], v25, v34, a[0:3]
	v_mfma_f32_16x16x4_f32 a[4:7], v25, v46, a[4:7]
	v_mfma_f32_16x16x4_f32 a[0:3], v2, v10, a[0:3]
	v_mov_b32_e32 v10, v27
	s_nop 0
	v_mfma_f32_16x16x4_f32 a[4:7], v2, v23, a[4:7]
	v_mfma_f32_16x16x4_f32 a[0:3], v3, v11, a[0:3]
	v_mfma_f32_16x16x4_f32 a[4:7], v3, v10, a[4:7]
	v_mfma_f32_16x16x4_f32 a[0:3], v4, v12, a[0:3]
	v_mfma_f32_16x16x4_f32 a[4:7], v4, v28, a[4:7]
	v_mfma_f32_16x16x4_f32 a[0:3], v5, v13, a[0:3]
	v_mfma_f32_16x16x4_f32 a[4:7], v5, v22, a[4:7]
	global_load_dwordx4 v[70:73], v[110:111], off offset:1024 nt
	global_load_dwordx4 v[34:37], v[110:111], off offset:1088 nt
	global_load_dwordx4 v[140:143], v[114:115], off offset:1024
	global_load_dwordx4 v[46:49], v[114:115], off offset:1088
	global_load_dwordx4 v[144:147], v[112:113], off offset:1024
	global_load_dwordx4 v[74:77], v[112:113], off offset:1088
	global_load_dwordx4 v[22:25], v[110:111], off offset:1152 nt
	global_load_dwordx4 v[2:5], v[110:111], off offset:1216 nt
	global_load_dwordx4 v[50:53], v[114:115], off offset:1152
	global_load_dwordx4 v[10:13], v[114:115], off offset:1216
	global_load_dwordx4 v[78:81], v[112:113], off offset:1152
	global_load_dwordx4 v[26:29], v[112:113], off offset:1216
	s_waitcnt vmcnt(21)
	v_mov_b32_e32 v82, v150
	v_mov_b32_e32 v150, v151
	s_waitcnt vmcnt(19)
	v_mov_b32_e32 v151, v155
	v_mfma_f32_16x16x4_f32 a[0:3], v54, v148, a[0:3]
	v_mov_b32_e32 v148, v153
	s_nop 0
	v_mfma_f32_16x16x4_f32 a[4:7], v54, v152, a[4:7]
	v_mov_b32_e32 v54, v68
	v_mfma_f32_16x16x4_f32 a[0:3], v55, v149, a[0:3]
	v_mfma_f32_16x16x4_f32 a[4:7], v55, v148, a[4:7]
	v_mov_b32_e32 v55, v67
	v_mfma_f32_16x16x4_f32 a[0:3], v56, v82, a[0:3]
	v_mfma_f32_16x16x4_f32 a[4:7], v56, v154, a[4:7]
	v_mov_b32_e32 v56, v69
	v_mfma_f32_16x16x4_f32 a[0:3], v57, v150, a[0:3]
	v_mfma_f32_16x16x4_f32 a[4:7], v57, v151, a[4:7]
	s_waitcnt vmcnt(18)
	v_mov_b32_e32 v57, v61
	s_waitcnt vmcnt(17)
	v_mfma_f32_16x16x4_f32 a[0:3], v38, v66, a[0:3]
	v_mfma_f32_16x16x4_f32 a[4:7], v38, v58, a[4:7]
	s_waitcnt vmcnt(15)
	v_mov_b32_e32 v38, v43
	v_mfma_f32_16x16x4_f32 a[0:3], v39, v55, a[0:3]
	v_mfma_f32_16x16x4_f32 a[4:7], v39, v59, a[4:7]
	v_mov_b32_e32 v39, v45
	v_mfma_f32_16x16x4_f32 a[0:3], v40, v54, a[0:3]
	v_mfma_f32_16x16x4_f32 a[4:7], v40, v60, a[4:7]
	v_mov_b32_e32 v40, v42
	s_waitcnt vmcnt(13)
	v_mov_b32_e32 v42, v64
	v_mfma_f32_16x16x4_f32 a[0:3], v41, v56, a[0:3]
	v_mfma_f32_16x16x4_f32 a[4:7], v41, v57, a[4:7]
	v_mov_b32_e32 v41, v62
	v_mfma_f32_16x16x4_f32 a[0:3], v18, v40, a[0:3]
	v_mov_b32_e32 v40, v65
	s_nop 0
	v_mfma_f32_16x16x4_f32 a[4:7], v18, v41, a[4:7]
	s_waitcnt vmcnt(12)
	v_mov_b32_e32 v18, v30
	v_mfma_f32_16x16x4_f32 a[0:3], v19, v38, a[0:3]
	v_mfma_f32_16x16x4_f32 a[4:7], v19, v63, a[4:7]
	v_mov_b32_e32 v19, v32
	v_mfma_f32_16x16x4_f32 a[0:3], v20, v44, a[0:3]
	v_mfma_f32_16x16x4_f32 a[4:7], v20, v42, a[4:7]
	v_mfma_f32_16x16x4_f32 a[0:3], v21, v39, a[0:3]
	v_mfma_f32_16x16x4_f32 a[4:7], v21, v40, a[4:7]
	v_mfma_f32_16x16x4_f32 a[0:3], v6, v14, a[0:3]
	v_mov_b32_e32 v14, v33
	s_nop 0
	v_mfma_f32_16x16x4_f32 a[4:7], v6, v18, a[4:7]
	v_mfma_f32_16x16x4_f32 a[0:3], v7, v15, a[0:3]
	v_mfma_f32_16x16x4_f32 a[4:7], v7, v31, a[4:7]
	v_mfma_f32_16x16x4_f32 a[0:3], v8, v16, a[0:3]
	v_mfma_f32_16x16x4_f32 a[4:7], v8, v19, a[4:7]
	v_mfma_f32_16x16x4_f32 a[0:3], v9, v17, a[0:3]
	v_mfma_f32_16x16x4_f32 a[4:7], v9, v14, a[4:7]
	global_load_dwordx4 v[54:57], v[110:111], off offset:1280 nt
	global_load_dwordx4 v[38:41], v[110:111], off offset:1344 nt
	global_load_dwordx4 v[148:151], v[114:115], off offset:1280
	global_load_dwordx4 v[66:69], v[114:115], off offset:1344
	global_load_dwordx4 v[152:155], v[112:113], off offset:1280
	global_load_dwordx4 v[58:61], v[112:113], off offset:1344
	global_load_dwordx4 v[18:21], v[110:111], off offset:1408 nt
	global_load_dwordx4 v[6:9], v[110:111], off offset:1472 nt
	global_load_dwordx4 v[42:45], v[114:115], off offset:1408
	global_load_dwordx4 v[14:17], v[114:115], off offset:1472
	global_load_dwordx4 v[62:65], v[112:113], off offset:1408
	global_load_dwordx4 v[30:33], v[112:113], off offset:1472
	s_waitcnt vmcnt(21)
	v_mov_b32_e32 v82, v143
	s_waitcnt vmcnt(19)
	v_mov_b32_e32 v143, v146
	v_mfma_f32_16x16x4_f32 a[0:3], v70, v140, a[0:3]
	v_mov_b32_e32 v140, v144
	v_mov_b32_e32 v144, v145
	s_nop 0
	v_mfma_f32_16x16x4_f32 a[4:7], v70, v140, a[4:7]
	s_waitcnt vmcnt(18)
	v_mov_b32_e32 v70, v75
	v_mfma_f32_16x16x4_f32 a[0:3], v71, v141, a[0:3]
	v_mfma_f32_16x16x4_f32 a[4:7], v71, v144, a[4:7]
	v_mov_b32_e32 v71, v77
	v_mfma_f32_16x16x4_f32 a[0:3], v72, v142, a[0:3]
	v_mfma_f32_16x16x4_f32 a[4:7], v72, v143, a[4:7]
	v_mfma_f32_16x16x4_f32 a[0:3], v73, v82, a[0:3]
	v_mfma_f32_16x16x4_f32 a[4:7], v73, v147, a[4:7]
	v_mfma_f32_16x16x4_f32 a[0:3], v34, v46, a[0:3]
	v_mov_b32_e32 v46, v76
	s_waitcnt vmcnt(17)
	v_mfma_f32_16x16x4_f32 a[4:7], v34, v74, a[4:7]
	s_waitcnt vmcnt(15)
	v_mov_b32_e32 v34, v53
	v_mfma_f32_16x16x4_f32 a[0:3], v35, v47, a[0:3]
	v_mfma_f32_16x16x4_f32 a[4:7], v35, v70, a[4:7]
	v_mov_b32_e32 v35, v50
	v_mfma_f32_16x16x4_f32 a[0:3], v36, v48, a[0:3]
	v_mfma_f32_16x16x4_f32 a[4:7], v36, v46, a[4:7]
	v_mov_b32_e32 v36, v52
	s_waitcnt vmcnt(13)
	v_mov_b32_e32 v46, v81
	v_mfma_f32_16x16x4_f32 a[0:3], v37, v49, a[0:3]
	v_mfma_f32_16x16x4_f32 a[4:7], v37, v71, a[4:7]
	v_mov_b32_e32 v37, v79
	v_mfma_f32_16x16x4_f32 a[0:3], v22, v35, a[0:3]
	v_mov_b32_e32 v35, v80
	s_nop 0
	v_mfma_f32_16x16x4_f32 a[4:7], v22, v78, a[4:7]
	s_waitcnt vmcnt(12)
	v_mov_b32_e32 v22, v29
	v_mfma_f32_16x16x4_f32 a[0:3], v23, v51, a[0:3]
	v_mfma_f32_16x16x4_f32 a[4:7], v23, v37, a[4:7]
	v_mov_b32_e32 v23, v26
	v_mfma_f32_16x16x4_f32 a[0:3], v24, v36, a[0:3]
	v_mfma_f32_16x16x4_f32 a[4:7], v24, v35, a[4:7]
	v_mfma_f32_16x16x4_f32 a[0:3], v25, v34, a[0:3]
	v_mfma_f32_16x16x4_f32 a[4:7], v25, v46, a[4:7]
	v_mfma_f32_16x16x4_f32 a[0:3], v2, v10, a[0:3]
	v_mov_b32_e32 v10, v27
	s_nop 0
	v_mfma_f32_16x16x4_f32 a[4:7], v2, v23, a[4:7]
	v_mfma_f32_16x16x4_f32 a[0:3], v3, v11, a[0:3]
	v_mfma_f32_16x16x4_f32 a[4:7], v3, v10, a[4:7]
	v_mfma_f32_16x16x4_f32 a[0:3], v4, v12, a[0:3]
	v_mfma_f32_16x16x4_f32 a[4:7], v4, v28, a[4:7]
	v_mfma_f32_16x16x4_f32 a[0:3], v5, v13, a[0:3]
	v_mfma_f32_16x16x4_f32 a[4:7], v5, v22, a[4:7]
	global_load_dwordx4 v[70:73], v[110:111], off offset:1536 nt
	global_load_dwordx4 v[34:37], v[110:111], off offset:1600 nt
	global_load_dwordx4 v[140:143], v[114:115], off offset:1536
	global_load_dwordx4 v[46:49], v[114:115], off offset:1600
	global_load_dwordx4 v[144:147], v[112:113], off offset:1536
	global_load_dwordx4 v[74:77], v[112:113], off offset:1600
	global_load_dwordx4 v[22:25], v[110:111], off offset:1664 nt
	global_load_dwordx4 v[2:5], v[110:111], off offset:1728 nt
	global_load_dwordx4 v[50:53], v[114:115], off offset:1664
	global_load_dwordx4 v[10:13], v[114:115], off offset:1728
	global_load_dwordx4 v[78:81], v[112:113], off offset:1664
	global_load_dwordx4 v[26:29], v[112:113], off offset:1728
	s_waitcnt vmcnt(21)
	v_mov_b32_e32 v82, v150
	v_mov_b32_e32 v150, v151
	s_waitcnt vmcnt(19)
	v_mov_b32_e32 v151, v155
	v_mfma_f32_16x16x4_f32 a[0:3], v54, v148, a[0:3]
	v_mov_b32_e32 v148, v153
	s_nop 0
	v_mfma_f32_16x16x4_f32 a[4:7], v54, v152, a[4:7]
	v_mov_b32_e32 v54, v68
	v_mfma_f32_16x16x4_f32 a[0:3], v55, v149, a[0:3]
	v_mfma_f32_16x16x4_f32 a[4:7], v55, v148, a[4:7]
	v_mov_b32_e32 v55, v67
	v_mfma_f32_16x16x4_f32 a[0:3], v56, v82, a[0:3]
	v_mfma_f32_16x16x4_f32 a[4:7], v56, v154, a[4:7]
	v_mov_b32_e32 v56, v69
	v_mfma_f32_16x16x4_f32 a[0:3], v57, v150, a[0:3]
	v_mfma_f32_16x16x4_f32 a[4:7], v57, v151, a[4:7]
	s_waitcnt vmcnt(18)
	v_mov_b32_e32 v57, v61
	s_waitcnt vmcnt(17)
	v_mfma_f32_16x16x4_f32 a[0:3], v38, v66, a[0:3]
	v_mfma_f32_16x16x4_f32 a[4:7], v38, v58, a[4:7]
	s_waitcnt vmcnt(15)
	v_mov_b32_e32 v38, v43
	v_mfma_f32_16x16x4_f32 a[0:3], v39, v55, a[0:3]
	v_mfma_f32_16x16x4_f32 a[4:7], v39, v59, a[4:7]
	v_mov_b32_e32 v39, v45
	v_mfma_f32_16x16x4_f32 a[0:3], v40, v54, a[0:3]
	v_mfma_f32_16x16x4_f32 a[4:7], v40, v60, a[4:7]
	v_mov_b32_e32 v40, v42
	s_waitcnt vmcnt(13)
	v_mov_b32_e32 v42, v64
	v_mfma_f32_16x16x4_f32 a[0:3], v41, v56, a[0:3]
	v_mfma_f32_16x16x4_f32 a[4:7], v41, v57, a[4:7]
	v_mov_b32_e32 v41, v62
	v_mfma_f32_16x16x4_f32 a[0:3], v18, v40, a[0:3]
	v_mov_b32_e32 v40, v65
	s_nop 0
	v_mfma_f32_16x16x4_f32 a[4:7], v18, v41, a[4:7]
	s_waitcnt vmcnt(12)
	v_mov_b32_e32 v18, v30
	v_mfma_f32_16x16x4_f32 a[0:3], v19, v38, a[0:3]
	v_mfma_f32_16x16x4_f32 a[4:7], v19, v63, a[4:7]
	v_mov_b32_e32 v19, v32
	v_mfma_f32_16x16x4_f32 a[0:3], v20, v44, a[0:3]
	v_mfma_f32_16x16x4_f32 a[4:7], v20, v42, a[4:7]
	v_mfma_f32_16x16x4_f32 a[0:3], v21, v39, a[0:3]
	v_mfma_f32_16x16x4_f32 a[4:7], v21, v40, a[4:7]
	v_mfma_f32_16x16x4_f32 a[0:3], v6, v14, a[0:3]
	v_mov_b32_e32 v14, v33
	s_nop 0
	v_mfma_f32_16x16x4_f32 a[4:7], v6, v18, a[4:7]
	v_mfma_f32_16x16x4_f32 a[0:3], v7, v15, a[0:3]
	v_mfma_f32_16x16x4_f32 a[4:7], v7, v31, a[4:7]
	v_mfma_f32_16x16x4_f32 a[0:3], v8, v16, a[0:3]
	v_mfma_f32_16x16x4_f32 a[4:7], v8, v19, a[4:7]
	v_mfma_f32_16x16x4_f32 a[0:3], v9, v17, a[0:3]
	v_mfma_f32_16x16x4_f32 a[4:7], v9, v14, a[4:7]
	global_load_dwordx4 v[6:9], v[110:111], off offset:1792 nt
	global_load_dwordx4 v[14:17], v[110:111], off offset:1856 nt
	global_load_dwordx4 v[18:21], v[114:115], off offset:1792
	global_load_dwordx4 v[30:33], v[114:115], off offset:1856
	global_load_dwordx4 v[38:41], v[112:113], off offset:1792
	global_load_dwordx4 v[42:45], v[112:113], off offset:1856
	global_load_dwordx4 v[54:57], v[110:111], off offset:1920 nt
	global_load_dwordx4 v[58:61], v[110:111], off offset:1984 nt
	global_load_dwordx4 v[62:65], v[114:115], off offset:1920
	global_load_dwordx4 v[66:69], v[114:115], off offset:1984
	global_load_dwordx4 v[148:151], v[112:113], off offset:1920
	s_nop 0
	global_load_dwordx4 v[112:115], v[112:113], off offset:1984
	s_waitcnt vmcnt(21)
	v_mov_b32_e32 v82, v143
	s_waitcnt vmcnt(19)
	v_mov_b32_e32 v143, v146
	v_mfma_f32_16x16x4_f32 a[0:3], v70, v140, a[0:3]
	v_mov_b32_e32 v140, v144
	v_mov_b32_e32 v144, v145
	s_nop 0
	v_mfma_f32_16x16x4_f32 a[4:7], v70, v140, a[4:7]
	s_waitcnt vmcnt(18)
	v_mov_b32_e32 v70, v75
	v_mfma_f32_16x16x4_f32 a[0:3], v71, v141, a[0:3]
	v_mfma_f32_16x16x4_f32 a[4:7], v71, v144, a[4:7]
	v_mov_b32_e32 v71, v77
	v_mfma_f32_16x16x4_f32 a[0:3], v72, v142, a[0:3]
	v_mfma_f32_16x16x4_f32 a[4:7], v72, v143, a[4:7]
	v_mfma_f32_16x16x4_f32 a[0:3], v73, v82, a[0:3]
	v_mfma_f32_16x16x4_f32 a[4:7], v73, v147, a[4:7]
	v_mfma_f32_16x16x4_f32 a[0:3], v34, v46, a[0:3]
	v_mov_b32_e32 v46, v76
	s_waitcnt vmcnt(17)
	v_mfma_f32_16x16x4_f32 a[4:7], v34, v74, a[4:7]
	s_waitcnt vmcnt(15)
	v_mov_b32_e32 v34, v53
	v_mfma_f32_16x16x4_f32 a[0:3], v35, v47, a[0:3]
	v_mfma_f32_16x16x4_f32 a[4:7], v35, v70, a[4:7]
	v_mov_b32_e32 v35, v50
	v_mfma_f32_16x16x4_f32 a[0:3], v36, v48, a[0:3]
	v_mfma_f32_16x16x4_f32 a[4:7], v36, v46, a[4:7]
	v_mov_b32_e32 v36, v52
	s_waitcnt vmcnt(13)
	v_mov_b32_e32 v46, v81
	v_mfma_f32_16x16x4_f32 a[0:3], v37, v49, a[0:3]
	v_mfma_f32_16x16x4_f32 a[4:7], v37, v71, a[4:7]
	v_mov_b32_e32 v37, v79
	v_mfma_f32_16x16x4_f32 a[0:3], v22, v35, a[0:3]
	v_mov_b32_e32 v35, v80
	s_nop 0
	v_mfma_f32_16x16x4_f32 a[4:7], v22, v78, a[4:7]
	s_waitcnt vmcnt(12)
	v_mov_b32_e32 v22, v29
	v_mfma_f32_16x16x4_f32 a[0:3], v23, v51, a[0:3]
	v_mfma_f32_16x16x4_f32 a[4:7], v23, v37, a[4:7]
	v_mov_b32_e32 v23, v26
	v_mfma_f32_16x16x4_f32 a[0:3], v24, v36, a[0:3]
	v_mfma_f32_16x16x4_f32 a[4:7], v24, v35, a[4:7]
	v_mfma_f32_16x16x4_f32 a[0:3], v25, v34, a[0:3]
	v_mfma_f32_16x16x4_f32 a[4:7], v25, v46, a[4:7]
	v_mfma_f32_16x16x4_f32 a[0:3], v2, v10, a[0:3]
	v_mov_b32_e32 v10, v27
	s_nop 0
	v_mfma_f32_16x16x4_f32 a[4:7], v2, v23, a[4:7]
	v_mfma_f32_16x16x4_f32 a[0:3], v3, v11, a[0:3]
	v_mfma_f32_16x16x4_f32 a[4:7], v3, v10, a[4:7]
	v_mfma_f32_16x16x4_f32 a[0:3], v4, v12, a[0:3]
	v_mfma_f32_16x16x4_f32 a[4:7], v4, v28, a[4:7]
	v_mfma_f32_16x16x4_f32 a[0:3], v5, v13, a[0:3]
	v_mfma_f32_16x16x4_f32 a[4:7], v5, v22, a[4:7]
	s_waitcnt vmcnt(11)
	v_mov_b32_e32 v2, v9
	v_mov_b32_e32 v3, v6
	v_mov_b32_e32 v4, v8
	s_waitcnt vmcnt(9)
	v_mov_b32_e32 v5, v20
	v_mov_b32_e32 v6, v19
	v_mov_b32_e32 v8, v21
	s_waitcnt vmcnt(7)
	v_mov_b32_e32 v9, v39
	v_mfma_f32_16x16x4_f32 a[0:3], v3, v18, a[0:3]
	v_mov_b32_e32 v10, v41
	v_mov_b32_e32 v11, v38
	s_nop 1
	v_mfma_f32_16x16x4_f32 a[4:7], v3, v11, a[4:7]
	v_mov_b32_e32 v3, v14
	v_mfma_f32_16x16x4_f32 a[0:3], v7, v6, a[0:3]
	v_mov_b32_e32 v6, v31
	v_mfma_f32_16x16x4_f32 a[4:7], v7, v9, a[4:7]
	v_mov_b32_e32 v7, v33
	s_waitcnt vmcnt(6)
	v_mov_b32_e32 v9, v42
	v_mfma_f32_16x16x4_f32 a[0:3], v4, v5, a[0:3]
	v_mov_b32_e32 v5, v32
	v_mfma_f32_16x16x4_f32 a[4:7], v4, v40, a[4:7]
	v_mov_b32_e32 v4, v16
	v_mfma_f32_16x16x4_f32 a[0:3], v2, v8, a[0:3]
	v_mov_b32_e32 v8, v45
	v_mfma_f32_16x16x4_f32 a[4:7], v2, v10, a[4:7]
	v_mov_b32_e32 v2, v17
	v_mov_b32_e32 v10, v44
	v_mfma_f32_16x16x4_f32 a[0:3], v3, v30, a[0:3]
	v_mfma_f32_16x16x4_f32 a[4:7], v3, v9, a[4:7]
	s_waitcnt vmcnt(5)
	v_mov_b32_e32 v3, v56
	s_waitcnt vmcnt(1)
	v_mov_b32_e32 v9, v150
	v_mfma_f32_16x16x4_f32 a[0:3], v15, v6, a[0:3]
	v_mov_b32_e32 v6, v65
	v_mfma_f32_16x16x4_f32 a[4:7], v15, v43, a[4:7]
	v_mfma_f32_16x16x4_f32 a[0:3], v4, v5, a[0:3]
	v_mov_b32_e32 v5, v63
	v_mfma_f32_16x16x4_f32 a[4:7], v4, v10, a[4:7]
	v_mov_b32_e32 v4, v55
	v_mfma_f32_16x16x4_f32 a[0:3], v2, v7, a[0:3]
	v_mov_b32_e32 v7, v62
	v_mfma_f32_16x16x4_f32 a[4:7], v2, v8, a[4:7]
	v_mov_b32_e32 v2, v54
	v_mov_b32_e32 v8, v148
	s_nop 0
	v_mfma_f32_16x16x4_f32 a[0:3], v2, v7, a[0:3]
	v_mov_b32_e32 v7, v151
	s_nop 0
	v_mfma_f32_16x16x4_f32 a[4:7], v2, v8, a[4:7]
	v_mov_b32_e32 v2, v60
	s_waitcnt vmcnt(0)
	v_mov_b32_e32 v8, v112
	v_mfma_f32_16x16x4_f32 a[0:3], v4, v5, a[0:3]
	v_mov_b32_e32 v5, v69
	v_mfma_f32_16x16x4_f32 a[4:7], v4, v149, a[4:7]
	v_mov_b32_e32 v4, v67
	v_mfma_f32_16x16x4_f32 a[0:3], v3, v64, a[0:3]
	v_mfma_f32_16x16x4_f32 a[4:7], v3, v9, a[4:7]
	v_mov_b32_e32 v3, v59
	v_mov_b32_e32 v9, v114
	v_mfma_f32_16x16x4_f32 a[0:3], v57, v6, a[0:3]
	v_mov_b32_e32 v6, v61
	v_mfma_f32_16x16x4_f32 a[4:7], v57, v7, a[4:7]
	v_mov_b32_e32 v7, v66
	s_nop 1
	v_mfma_f32_16x16x4_f32 a[0:3], v58, v7, a[0:3]
	v_mov_b32_e32 v7, v115
	v_mfma_f32_16x16x4_f32 a[0:3], v3, v4, a[0:3]
	v_mfma_f32_16x16x4_f32 a[4:7], v58, v8, a[4:7]
	v_mfma_f32_16x16x4_f32 a[0:3], v2, v68, a[0:3]
	v_mfma_f32_16x16x4_f32 a[4:7], v3, v113, a[4:7]
	v_mfma_f32_16x16x4_f32 a[0:3], v6, v5, a[0:3]
	v_mfma_f32_16x16x4_f32 a[4:7], v2, v9, a[4:7]
	s_nop 8
	v_accvgpr_read_b32 v5, a3
	v_accvgpr_read_b32 v4, a2
	v_accvgpr_read_b32 v3, a1
	v_accvgpr_read_b32 v2, a0
	v_mfma_f32_16x16x4_f32 a[0:3], v6, v7, a[4:7]
	v_or_b32_e32 v6, v129, v139
	v_ashrrev_i32_e32 v7, 31, v6
	v_lshl_add_u64 v[6:7], v[6:7], 2, s[24:25]
	global_load_dword v6, v[6:7], off
	s_and_saveexec_b64 s[0:1], s[10:11]
	s_cbranch_execnz .LBB2_43
	s_or_b64 exec, exec, s[0:1]
	s_and_saveexec_b64 s[0:1], s[12:13]
	s_cbranch_execnz .LBB2_44
